# baseline (speedup 1.0000x reference)
_Z11attn_kernelPKDF16_S0_S0_PDF16_:
	s_bfe_u32 s26, s2, 0x20003
	s_load_dwordx8 s[4:11], s[0:1], 0x0
	s_lshr_b32 s1, s2, 2
	s_lshr_b32 s20, s2, 6
	v_readfirstlane_b32 s19, v0
	s_mov_b32 s21, 0
	s_lshl_b32 s27, s26, 8
	s_and_b32 s0, s2, 7
	s_and_b32 s1, s1, 8
	s_lshr_b32 s34, s19, 6
	s_lshr_b32 s55, s19, 6
	s_lshl_b32 s56, s55, 5
	s_add_i32 s50, s56, 222
	s_add_i32 s51, s56, 190
	s_add_i32 s52, s56, 158
	s_add_i32 s53, s56, 126
	s_add_i32 s54, s56, 94
	s_add_i32 s56, s56, 62
	s_lshl_b64 s[12:13], s[20:21], 11
	s_xor_b32 s16, s27, 0x700
	s_or_b32 s18, s1, s0
	s_or_b32 s0, s12, s16
	s_lshl_b32 s24, s34, 5
	s_add_u32 s0, s0, s24
	s_addc_u32 s1, s13, 0
	s_lshl_b64 s[14:15], s[0:1], 10
	s_lshl_b64 s[0:1], s[0:1], 11
	s_waitcnt lgkmcnt(0)
	s_add_u32 s0, s4, s0
	s_addc_u32 s1, s5, s1
	s_lshl_b32 s33, s18, 6
	s_lshl_b32 s2, s18, 7
	s_add_u32 s2, s0, s2
	s_addc_u32 s3, s1, 0
	s_lshl_b32 s0, s20, 4
	s_or_b32 s20, s18, s0
	s_and_b32 s17, s19, 0x3fffffc0
	s_lshl_b64 s[0:1], s[20:21], 18
	s_add_u32 s28, s6, s0
	s_addc_u32 s29, s7, s1
	s_lshl_b32 s18, s34, 10
	s_add_u32 s6, s28, s18
	s_addc_u32 s7, s29, 0
	s_add_u32 s30, s8, s0
	s_addc_u32 s31, s9, s1
	s_lshl_b32 s0, s19, 4
	v_and_b32_e32 v207, 63, v0
	s_and_b32 s0, s0, 0xfffff000
	v_mov_b32_e32 v3, 0
	v_lshlrev_b32_e32 v2, 4, v207
	s_add_u32 s0, s30, s0
	v_lshl_add_u64 v[212:213], s[6:7], 0, v[2:3]
	s_addc_u32 s1, s31, 0
	s_lshr_b32 s6, s19, 2
	v_bfe_u32 v1, v0, 2, 4
	v_and_or_b32 v2, s6, 48, v1
	v_lshlrev_b32_e32 v2, 6, v2
	v_lshlrev_b32_e32 v209, 3, v0
	s_cmp_lg_u32 0, -1
	v_lshl_add_u64 v[4:5], s[0:1], 0, v[2:3]
	v_and_b32_e32 v208, 24, v209
	s_cselect_b32 s0, 0, 0
	v_and_b32_e32 v222, 31, v0
	v_lshlrev_b32_e32 v2, 1, v208
	s_add_i32 s35, s18, s0
	s_mov_b32 s0, m0
	s_mov_b32 m0, s35
	s_nop 0
	global_load_lds_dwordx4 v[212:213], off
	s_mov_b32 m0, s0
	v_bfe_u32 v211, v0, 5, 1
	v_lshl_add_u64 v[194:195], v[4:5], 0, v[2:3]
	s_add_i32 s39, s35, 0x6000
	s_mov_b32 s0, m0
	s_mov_b32 m0, s39
	s_nop 0
	global_load_lds_dwordx4 v[194:195], off
	s_mov_b32 m0, s0
	v_lshlrev_b32_e32 v2, 10, v222
	s_mov_b64 s[0:1], 0x2000
	v_lshl_or_b32 v210, v211, 3, v2
	v_lshl_add_u64 v[214:215], v[212:213], 0, s[0:1]
	s_add_i32 s36, s35, 0x2000
	s_mov_b32 s6, m0
	s_mov_b32 m0, s36
	s_nop 0
	global_load_lds_dwordx4 v[214:215], off
	s_mov_b32 m0, s6
	v_lshlrev_b32_e32 v2, 1, v210
	global_load_dwordx4 v[158:161], v2, s[2:3]
	global_load_dwordx4 v[154:157], v2, s[2:3] offset:32
	global_load_dwordx4 v[150:153], v2, s[2:3] offset:64
	global_load_dwordx4 v[146:149], v2, s[2:3] offset:96
	v_lshlrev_b32_e32 v4, 10, v211
	v_lshlrev_b32_e32 v5, 4, v222
	v_add3_u32 v224, 0, v4, v5
	v_mov_b32_e32 v4, v3
	v_mov_b32_e32 v5, v3
	v_mov_b32_e32 v6, v3
	v_mov_b32_e32 v7, v3
	v_mov_b32_e32 v8, v3
	v_mov_b32_e32 v9, v3
	v_mov_b32_e32 v10, v3
	v_mov_b32_e32 v11, v3
	v_mov_b32_e32 v12, v3
	v_mov_b32_e32 v13, v3
	v_mov_b32_e32 v14, v3
	v_mov_b32_e32 v15, v3
	v_mov_b32_e32 v16, v3
	v_mov_b32_e32 v17, v3
	v_mov_b32_e32 v18, v3
	v_mov_b32_e32 v19, v3
	s_mov_b64 s[2:3], 0x4000
	s_add_i32 s37, s35, 0x4000
	v_lshl_add_u64 v[216:217], v[212:213], 0, s[2:3]
	s_mov_b32 s6, m0
	s_mov_b32 m0, s37
	s_nop 0
	global_load_lds_dwordx4 v[216:217], off
	s_mov_b32 m0, s6
	s_waitcnt vmcnt(3) lgkmcnt(0)
	s_barrier
	ds_read_b128 v[36:39], v224
	ds_read_b128 v[40:43], v224 offset:512
	s_mov_b64 s[6:7], 0x6000
	s_mov_b32 s41, 3
	s_movk_i32 s46, 0x2000
	s_movk_i32 s25, 0x4000
	s_sub_i32 s43, 0xbf, s16
	s_mov_b32 s45, 0x41000000
	s_mov_b64 s[18:19], 0xa000
	v_lshlrev_b32_e32 v226, 4, v211
	v_mov_b32_e32 v233, v3
	v_lshlrev_b32_e32 v206, 3, v207
	s_waitcnt vmcnt(3) lgkmcnt(1)
	v_mfma_f32_32x32x16_f16 v[20:35], v[36:39], v[158:161], v[4:19]
	s_waitcnt lgkmcnt(0)
	v_mfma_f32_32x32x16_f16 v[4:19], v[40:43], v[158:161], v[4:19]
	ds_read_b128 v[36:39], v224 offset:2048
	ds_read_b128 v[40:43], v224 offset:2560
	s_waitcnt vmcnt(2) lgkmcnt(1)
	v_mfma_f32_32x32x16_f16 v[20:35], v[36:39], v[154:157], v[20:35]
	s_waitcnt lgkmcnt(0)
	v_mfma_f32_32x32x16_f16 v[4:19], v[40:43], v[154:157], v[4:19]
	ds_read_b128 v[36:39], v224 offset:4096
	ds_read_b128 v[40:43], v224 offset:4608
	s_waitcnt vmcnt(1) lgkmcnt(1)
	v_mfma_f32_32x32x16_f16 v[20:35], v[36:39], v[150:153], v[20:35]
	s_waitcnt lgkmcnt(0)
	v_mfma_f32_32x32x16_f16 v[4:19], v[40:43], v[150:153], v[4:19]
	ds_read_b128 v[36:39], v224 offset:6144
	ds_read_b128 v[40:43], v224 offset:6656
	s_waitcnt vmcnt(0) lgkmcnt(1)
	v_mfma_f32_32x32x16_f16 v[20:35], v[36:39], v[146:149], v[20:35]
	s_waitcnt lgkmcnt(0)
	v_mfma_f32_32x32x16_f16 v[4:19], v[40:43], v[146:149], v[4:19]
	s_nop 15
	s_nop 7
	s_nop 0
	v_max3_f32 v2, v20, v21, v4
	v_max3_f32 v36, v22, v23, v5
	s_nop 0
	v_max3_f32 v2, v2, v6, v7
	v_max3_f32 v36, v36, v26, v27
	s_nop 0
	v_max3_f32 v2, v2, v24, v25
	v_max3_f32 v36, v36, v10, v11
	s_nop 0
	v_max3_f32 v2, v2, v8, v9
	v_max3_f32 v36, v36, v30, v31
	s_nop 0
	v_max3_f32 v2, v2, v28, v29
	v_max3_f32 v36, v36, v14, v15
	s_nop 0
	v_max3_f32 v2, v2, v12, v13
	v_max3_f32 v36, v36, v34, v35
	s_nop 0
	v_max3_f32 v2, v2, v32, v33
	v_max3_f32 v36, v36, v18, v19
	s_nop 0
	v_max3_f32 v2, v2, v16, v17
	s_nop 0
	v_max_f32_e32 v2, v2, v36
	s_nop 0
	v_mov_b32_e32 v36, v2
	s_nop 1
	v_permlane32_swap_b32_e32 v2, v36
	v_max_f32_e32 v2, v2, v36
	s_nop 0
	v_sub_f32_e32 v50, v34, v2
	v_add_f32_e32 v231, v3, v2
	v_sub_f32_e32 v51, v35, v2
	v_sub_f32_e32 v52, v4, v2
	v_sub_f32_e32 v53, v5, v2
	v_lshl_add_u64 v[4:5], v[212:213], 0, s[6:7]
	v_xor_b32_e32 v34, 0x80000000, v231
	v_mov_b32_e32 v35, v34
	v_mov_b32_e32 v36, v34
	v_mov_b32_e32 v37, v34
	v_mov_b32_e32 v38, v34
	v_mov_b32_e32 v39, v34
	v_mov_b32_e32 v40, v34
	v_mov_b32_e32 v41, v34
	v_mov_b32_e32 v42, v34
	v_mov_b32_e32 v43, v34
	v_mov_b32_e32 v44, v34
	v_mov_b32_e32 v45, v34
	v_mov_b32_e32 v46, v34
	v_mov_b32_e32 v47, v34
	v_mov_b32_e32 v48, v34
	v_mov_b32_e32 v49, v34
	s_waitcnt vmcnt(0) lgkmcnt(0)
	s_barrier
	s_mov_b32 s8, m0
	s_mov_b32 m0, s35
	s_nop 0
	global_load_lds_dwordx4 v[4:5], off
	s_mov_b32 m0, s8
	s_add_i32 s8, s35, 0x8000
	v_lshl_add_u64 v[4:5], v[194:195], 0, s[0:1]
	s_mov_b32 s0, m0
	s_mov_b32 m0, s8
	s_nop 0
	global_load_lds_dwordx4 v[4:5], off
	s_mov_b32 m0, s0
	ds_read_b128 v[190:193], v224 offset:8192
	ds_read_b128 v[186:189], v224 offset:8704
	ds_read_b128 v[182:185], v224 offset:10240
	ds_read_b128 v[178:181], v224 offset:10752
	ds_read_b128 v[174:177], v224 offset:12288
	ds_read_b128 v[170:173], v224 offset:12800
	ds_read_b128 v[166:169], v224 offset:14336
	ds_read_b128 v[162:165], v224 offset:14848
	v_sub_f32_e32 v20, v20, v2
	v_sub_f32_e32 v21, v21, v2
	v_sub_f32_e32 v22, v22, v2
	v_sub_f32_e32 v23, v23, v2
	v_sub_f32_e32 v24, v24, v2
	v_sub_f32_e32 v25, v25, v2
	v_sub_f32_e32 v26, v26, v2
	v_sub_f32_e32 v27, v27, v2
	v_sub_f32_e32 v28, v28, v2
	v_sub_f32_e32 v29, v29, v2
	v_sub_f32_e32 v30, v30, v2
	v_sub_f32_e32 v31, v31, v2
	v_sub_f32_e32 v32, v32, v2
	v_sub_f32_e32 v33, v33, v2
	v_sub_f32_e32 v6, v6, v2
	v_sub_f32_e32 v7, v7, v2
	v_sub_f32_e32 v8, v8, v2
	v_sub_f32_e32 v9, v9, v2
	v_sub_f32_e32 v10, v10, v2
	v_sub_f32_e32 v11, v11, v2
	v_sub_f32_e32 v12, v12, v2
	v_sub_f32_e32 v13, v13, v2
	v_sub_f32_e32 v14, v14, v2
	v_sub_f32_e32 v15, v15, v2
	v_sub_f32_e32 v16, v16, v2
	v_sub_f32_e32 v17, v17, v2
	v_sub_f32_e32 v18, v18, v2
	v_sub_f32_e32 v19, v19, v2
	v_lshlrev_b32_e32 v2, 1, v0
	v_and_b32_e32 v228, 32, v2
	v_lshlrev_b32_e32 v2, 4, v0
	v_exp_f32_e32 v81, v51
	v_exp_f32_e32 v66, v20
	v_exp_f32_e32 v67, v21
	v_exp_f32_e32 v68, v22
	v_exp_f32_e32 v69, v23
	v_exp_f32_e32 v70, v24
	v_exp_f32_e32 v71, v25
	v_exp_f32_e32 v72, v26
	v_exp_f32_e32 v73, v27
	v_exp_f32_e32 v74, v28
	v_exp_f32_e32 v75, v29
	v_exp_f32_e32 v76, v30
	v_exp_f32_e32 v77, v31
	v_exp_f32_e32 v78, v32
	v_exp_f32_e32 v79, v33
	v_exp_f32_e32 v80, v50
	v_exp_f32_e32 v65, v19
	v_exp_f32_e32 v50, v52
	v_exp_f32_e32 v51, v53
	v_exp_f32_e32 v52, v6
	v_exp_f32_e32 v53, v7
	v_exp_f32_e32 v54, v8
	v_exp_f32_e32 v55, v9
	v_exp_f32_e32 v56, v10
	v_exp_f32_e32 v57, v11
	v_exp_f32_e32 v58, v12
	v_exp_f32_e32 v59, v13
	v_exp_f32_e32 v60, v14
	v_exp_f32_e32 v61, v15
	v_exp_f32_e32 v62, v16
	v_exp_f32_e32 v63, v17
	v_exp_f32_e32 v64, v18
	v_and_b32_e32 v2, 0xc0, v2
	s_add_i32 s0, s16, 0x100
	v_lshl_or_b32 v230, v211, 8, v2
	v_add_u32_e32 v2, 0, v228
	v_mov_b32_e32 v16, v3
	v_mov_b32_e32 v17, v3
	s_lshr_b32 s42, s0, 6
	s_lshl_b32 s0, s17, 2
	s_waitcnt vmcnt(2) lgkmcnt(0)
	s_barrier
	v_add3_u32 v225, v2, v208, v230
	v_mov_b32_e32 v2, v3
	v_mov_b32_e32 v4, v3
	v_mov_b32_e32 v5, v3
	v_mov_b32_e32 v6, v3
	v_mov_b32_e32 v7, v3
	v_mov_b32_e32 v8, v3
	v_mov_b32_e32 v9, v3
	v_mov_b32_e32 v10, v3
	v_mov_b32_e32 v11, v3
	v_mov_b32_e32 v12, v3
	v_mov_b32_e32 v13, v3
	v_mov_b32_e32 v14, v3
	v_mov_b32_e32 v15, v3
	s_add_i32 s38, s0, 0
	v_mov_b64_e32 v[32:33], v[16:17]
	v_cmp_gt_u32_e64 s[0:1], 32, v207
	s_mov_b64 s[8:9], 0
	s_mov_b64 s[16:17], 0x8000
	v_lshl_add_u32 v223, v222, 2, s38
	v_mov_b64_e32 v[30:31], v[14:15]
	v_mov_b64_e32 v[28:29], v[12:13]
	v_mov_b64_e32 v[26:27], v[10:11]
	v_mov_b64_e32 v[24:25], v[8:9]
	v_mov_b64_e32 v[22:23], v[6:7]
	v_mov_b64_e32 v[20:21], v[4:5]
	v_mov_b64_e32 v[18:19], v[2:3]

.LBB2_17:
	v_add_u32_e32 v83, s25, v225
	ds_read_b64_tr_b16 v[198:199], v83 offset:24576
	ds_read_b64_tr_b16 v[200:201], v83 offset:25088
	s_waitcnt lgkmcnt(9)
	s_cmp_gt_i32 s43, s52
	s_cbranch_scc1 .Lbsk_6566
	v_mfma_f32_32x32x16_f16 v[114:129], v[190:193], v[158:161], v[34:49]
.Lbsk_6566:
	v_add_f32_e32 v84, v66, v67
	v_add_f32_e32 v84, v68, v84
	v_add_f32_e32 v84, v69, v84
	v_add_f32_e32 v84, v70, v84
	v_add_f32_e32 v84, v71, v84
	v_cvt_pk_f16_f32 v142, v66, v67
	v_cvt_pk_f16_f32 v143, v68, v69
	ds_read_b64_tr_b16 v[190:191], v83 offset:28672
	ds_read_b64_tr_b16 v[192:193], v83 offset:29184
	s_waitcnt lgkmcnt(10)
	s_cmp_gt_i32 s43, s53
	s_cbranch_scc1 .Lbsk_6583
	v_mfma_f32_32x32x16_f16 v[98:113], v[186:189], v[158:161], v[34:49]
.Lbsk_6583:
	v_add_f32_e32 v66, v72, v84
	v_add_f32_e32 v66, v73, v66
	v_add_f32_e32 v66, v74, v66
	v_add_f32_e32 v66, v75, v66
	v_cvt_pk_f16_f32 v144, v70, v71
	v_cvt_pk_f16_f32 v145, v72, v73
	ds_read_b64_tr_b16 v[194:195], v83 offset:25600
	ds_read_b64_tr_b16 v[196:197], v83 offset:26112
	s_waitcnt lgkmcnt(11)
	s_cmp_gt_i32 s43, s52
	s_cbranch_scc1 .Lbsk_6599
	v_mfma_f32_32x32x16_f16 v[114:129], v[182:185], v[154:157], v[114:129]
.Lbsk_6599:
	v_add_f32_e32 v66, v76, v66
	v_add_f32_e32 v66, v77, v66
	v_add_f32_e32 v66, v78, v66
	v_add_f32_e32 v66, v79, v66
	v_cvt_pk_f16_f32 v138, v74, v75
	v_cvt_pk_f16_f32 v139, v76, v77
	ds_read_b64_tr_b16 v[74:75], v83 offset:29696
	ds_read_b64_tr_b16 v[76:77], v83 offset:30208
	s_waitcnt lgkmcnt(12)
	s_cmp_gt_i32 s43, s53
	s_cbranch_scc1 .Lbsk_6615
	v_mfma_f32_32x32x16_f16 v[98:113], v[178:181], v[154:157], v[98:113]
.Lbsk_6615:
	v_add_f32_e32 v66, v80, v66
	v_add_f32_e32 v66, v81, v66
	v_add_f32_e32 v66, v50, v66
	v_add_f32_e32 v66, v51, v66
	v_cvt_pk_f16_f32 v140, v78, v79
	v_cvt_pk_f16_f32 v141, v80, v81
	ds_read_b64_tr_b16 v[70:71], v83 offset:26624
	ds_read_b64_tr_b16 v[72:73], v83 offset:27136
	s_waitcnt lgkmcnt(13)
	s_cmp_gt_i32 s43, s52
	s_cbranch_scc1 .Lbsk_6631
	v_mfma_f32_32x32x16_f16 v[114:129], v[174:177], v[150:153], v[114:129]
.Lbsk_6631:
	v_add_f32_e32 v66, v52, v66
	v_add_f32_e32 v66, v53, v66
	v_add_f32_e32 v66, v54, v66
	v_add_f32_e32 v78, v55, v66
	v_cvt_pk_f16_f32 v134, v50, v51
	v_cvt_pk_f16_f32 v135, v52, v53
	ds_read_b64_tr_b16 v[66:67], v83 offset:30720
	ds_read_b64_tr_b16 v[68:69], v83 offset:31232
	s_waitcnt lgkmcnt(14)
	s_cmp_gt_i32 s43, s53
	s_cbranch_scc1 .Lbsk_6647
	v_mfma_f32_32x32x16_f16 v[98:113], v[170:173], v[150:153], v[98:113]
.Lbsk_6647:
	v_add_f32_e32 v50, v56, v78
	v_add_f32_e32 v50, v57, v50
	v_add_f32_e32 v50, v58, v50
	v_add_f32_e32 v50, v59, v50
	v_cvt_pk_f16_f32 v136, v54, v55
	v_cvt_pk_f16_f32 v137, v56, v57
	ds_read_b64_tr_b16 v[54:55], v83 offset:27648
	ds_read_b64_tr_b16 v[56:57], v83 offset:28160
	s_waitcnt lgkmcnt(14)
	s_cmp_gt_i32 s43, s52
	s_cbranch_scc1 .Lbsk_6663
	v_mfma_f32_32x32x16_f16 v[114:129], v[166:169], v[146:149], v[114:129]
.Lbsk_6663:
	v_add_f32_e32 v50, v60, v50
	v_add_f32_e32 v50, v61, v50
	v_add_f32_e32 v50, v62, v50
	v_add_f32_e32 v78, v63, v50
	v_cvt_pk_f16_f32 v130, v58, v59
	v_cvt_pk_f16_f32 v131, v60, v61
	ds_read_b64_tr_b16 v[50:51], v83 offset:31744
	ds_read_b64_tr_b16 v[52:53], v83 offset:32256
	s_cmp_gt_i32 s43, s53
	s_cbranch_scc1 .Lbsk_6678
	v_mfma_f32_32x32x16_f16 v[98:113], v[162:165], v[146:149], v[98:113]
.Lbsk_6678:
	v_add_f32_e32 v58, v64, v78
	v_add_f32_e32 v58, v65, v58
	v_add_f32_e32 v58, 0, v58
	v_cvt_pk_f16_f32 v132, v62, v63
	v_cvt_pk_f16_f32 v133, v64, v65
	s_add_i32 s2, s48, 1
	s_cmp_ge_u32 s2, s42
	s_cselect_b64 s[18:19], -1, 0
	s_and_b64 vcc, exec, s[18:19]
	s_cbranch_vccnz .LBB2_19
	v_lshl_add_u64 v[60:61], v[218:219], 0, s[8:9]
	s_add_i32 s2, s40, s35
	s_mov_b32 s3, m0
	s_mov_b32 m0, s2
	s_nop 0
	global_load_lds_dwordx4 v[60:61], off
	s_mov_b32 m0, s3

.LBB2_33:
	s_waitcnt lgkmcnt(14)
	s_cmp_gt_i32 s43, s50
	s_cbranch_scc1 .Lbsk_6957
	v_mfma_f32_32x32x16_f16 v[2:17], v[142:145], v[198:201], v[2:17]
.Lbsk_6957:
	v_exp_f32_e32 v114, v114
	v_exp_f32_e32 v115, v115
	v_exp_f32_e32 v116, v116
	v_exp_f32_e32 v117, v117
	s_waitcnt lgkmcnt(12)
	s_cmp_gt_i32 s43, s50
	s_cbranch_scc1 .Lbsk_6966
	v_mfma_f32_32x32x16_f16 v[18:33], v[142:145], v[190:193], v[18:33]
.Lbsk_6966:
	v_exp_f32_e32 v118, v118
	v_exp_f32_e32 v119, v119
	v_exp_f32_e32 v120, v120
	v_exp_f32_e32 v121, v121
	v_add_u32_e32 v58, s44, v224
	ds_read_b128 v[190:193], v58
	ds_read_b128 v[186:189], v58 offset:512
	s_waitcnt lgkmcnt(12)
	s_cmp_gt_i32 s43, s50
	s_cbranch_scc1 .Lbsk_6979
	v_mfma_f32_32x32x16_f16 v[2:17], v[138:141], v[194:197], v[2:17]
.Lbsk_6979:
	v_exp_f32_e32 v122, v122
	v_exp_f32_e32 v123, v123
	v_exp_f32_e32 v124, v124
	v_exp_f32_e32 v125, v125
	ds_read_b128 v[182:185], v58 offset:2048
	ds_read_b128 v[178:181], v58 offset:2560
	s_waitcnt lgkmcnt(12)
	s_cmp_gt_i32 s43, s50
	s_cbranch_scc1 .Lbsk_6991
	v_mfma_f32_32x32x16_f16 v[18:33], v[138:141], v[74:77], v[18:33]
.Lbsk_6991:
	v_exp_f32_e32 v126, v126
	v_exp_f32_e32 v127, v127
	v_exp_f32_e32 v128, v128
	v_exp_f32_e32 v129, v129
	ds_read_b128 v[174:177], v58 offset:4096
	ds_read_b128 v[170:173], v58 offset:4608
	s_waitcnt lgkmcnt(12)
	s_cmp_gt_i32 s43, s51
	s_cbranch_scc1 .Lbsk_7003
	v_mfma_f32_32x32x16_f16 v[2:17], v[134:137], v[70:73], v[2:17]
.Lbsk_7003:
	v_exp_f32_e32 v98, v98
	v_exp_f32_e32 v99, v99
	v_exp_f32_e32 v100, v100
	v_exp_f32_e32 v101, v101
	ds_read_b128 v[166:169], v58 offset:6144
	ds_read_b128 v[162:165], v58 offset:6656
	s_waitcnt lgkmcnt(12)
	s_cmp_gt_i32 s43, s51
	s_cbranch_scc1 .Lbsk_7015
	v_mfma_f32_32x32x16_f16 v[18:33], v[134:137], v[66:69], v[18:33]
.Lbsk_7015:
	v_exp_f32_e32 v102, v102
	v_exp_f32_e32 v103, v103
	v_exp_f32_e32 v104, v104
	v_exp_f32_e32 v105, v105
	s_waitcnt lgkmcnt(10)
	s_cmp_gt_i32 s43, s51
	s_cbranch_scc1 .Lbsk_7024
	v_mfma_f32_32x32x16_f16 v[2:17], v[130:133], v[54:57], v[2:17]
.Lbsk_7024:
	v_exp_f32_e32 v106, v106
	v_exp_f32_e32 v107, v107
	v_exp_f32_e32 v108, v108
	v_exp_f32_e32 v109, v109
	s_waitcnt lgkmcnt(8)
	s_cmp_gt_i32 s43, s51
	s_cbranch_scc1 .Lbsk_7033
	v_mfma_f32_32x32x16_f16 v[18:33], v[130:133], v[50:53], v[18:33]
.Lbsk_7033:
	v_exp_f32_e32 v110, v110
	v_exp_f32_e32 v111, v111
	v_exp_f32_e32 v112, v112
	v_exp_f32_e32 v113, v113
	s_mov_b64 s[20:21], -1
	s_and_b64 vcc, exec, s[18:19]
	s_cbranch_vccnz .LBB2_52
	s_andn2_b64 vcc, exec, s[20:21]
	s_cbranch_vccz .LBB2_57

.LBB2_37:
	v_add_u32_e32 v83, s40, v225
	ds_read_b64_tr_b16 v[202:203], v83 offset:24576
	ds_read_b64_tr_b16 v[204:205], v83 offset:25088
	s_waitcnt lgkmcnt(9)
	s_cmp_gt_i32 s43, s54
	s_cbranch_scc1 .Lbsk_7085
	v_mfma_f32_32x32x16_f16 v[66:81], v[190:193], v[158:161], v[34:49]
.Lbsk_7085:
	v_add_f32_e32 v50, v114, v115
	v_add_f32_e32 v50, v116, v50
	v_add_f32_e32 v50, v117, v50
	v_add_f32_e32 v50, v118, v50
	v_add_f32_e32 v50, v119, v50
	v_cvt_pk_f16_f32 v142, v114, v115
	v_cvt_pk_f16_f32 v143, v116, v117
	ds_read_b64_tr_b16 v[198:199], v83 offset:28672
	ds_read_b64_tr_b16 v[200:201], v83 offset:29184
	v_add_f32_e32 v50, v120, v50
	v_add_f32_e32 v50, v121, v50
	v_add_f32_e32 v50, v122, v50
	v_add_f32_e32 v84, v123, v50
	s_waitcnt lgkmcnt(10)
	s_cmp_gt_i32 s43, s56
	s_cbranch_scc1 .Lbsk_7106
	v_mfma_f32_32x32x16_f16 v[50:65], v[186:189], v[158:161], v[34:49]
.Lbsk_7106:
	v_cvt_pk_f16_f32 v144, v118, v119
	v_cvt_pk_f16_f32 v145, v120, v121
	ds_read_b64_tr_b16 v[194:195], v83 offset:25600
	ds_read_b64_tr_b16 v[196:197], v83 offset:26112
	s_waitcnt lgkmcnt(11)
	s_cmp_gt_i32 s43, s54
	s_cbranch_scc1 .Lbsk_7118
	v_mfma_f32_32x32x16_f16 v[66:81], v[182:185], v[154:157], v[66:81]
.Lbsk_7118:
	v_add_f32_e32 v84, v124, v84
	v_add_f32_e32 v84, v125, v84
	v_add_f32_e32 v84, v126, v84
	v_add_f32_e32 v84, v127, v84
	v_cvt_pk_f16_f32 v138, v122, v123
	v_cvt_pk_f16_f32 v139, v124, v125
	ds_read_b64_tr_b16 v[122:123], v83 offset:29696
	ds_read_b64_tr_b16 v[124:125], v83 offset:30208
	s_waitcnt lgkmcnt(12)
	s_cmp_gt_i32 s43, s56
	s_cbranch_scc1 .Lbsk_7134
	v_mfma_f32_32x32x16_f16 v[50:65], v[178:181], v[154:157], v[50:65]
.Lbsk_7134:
	v_add_f32_e32 v84, v128, v84
	v_add_f32_e32 v84, v129, v84
	v_add_f32_e32 v84, v98, v84
	v_add_f32_e32 v84, v99, v84
	v_cvt_pk_f16_f32 v140, v126, v127
	v_cvt_pk_f16_f32 v141, v128, v129
	ds_read_b64_tr_b16 v[118:119], v83 offset:26624
	ds_read_b64_tr_b16 v[120:121], v83 offset:27136
	s_waitcnt lgkmcnt(13)
	s_cmp_gt_i32 s43, s54
	s_cbranch_scc1 .Lbsk_7150
	v_mfma_f32_32x32x16_f16 v[66:81], v[174:177], v[150:153], v[66:81]
.Lbsk_7150:
	v_add_f32_e32 v84, v100, v84
	v_add_f32_e32 v84, v101, v84
	v_add_f32_e32 v84, v102, v84
	v_add_f32_e32 v84, v103, v84
	v_cvt_pk_f16_f32 v134, v98, v99
	v_cvt_pk_f16_f32 v135, v100, v101
	ds_read_b64_tr_b16 v[114:115], v83 offset:30720
	ds_read_b64_tr_b16 v[116:117], v83 offset:31232
	s_waitcnt lgkmcnt(14)
	s_cmp_gt_i32 s43, s56
	s_cbranch_scc1 .Lbsk_7166
	v_mfma_f32_32x32x16_f16 v[50:65], v[170:173], v[150:153], v[50:65]
.Lbsk_7166:
	v_add_f32_e32 v84, v104, v84
	v_add_f32_e32 v84, v105, v84
	v_add_f32_e32 v84, v106, v84
	v_add_f32_e32 v84, v107, v84
	v_cvt_pk_f16_f32 v136, v102, v103
	v_cvt_pk_f16_f32 v137, v104, v105
	ds_read_b64_tr_b16 v[102:103], v83 offset:27648
	ds_read_b64_tr_b16 v[104:105], v83 offset:28160
	s_waitcnt lgkmcnt(14)
	s_cmp_gt_i32 s43, s54
	s_cbranch_scc1 .Lbsk_7182
	v_mfma_f32_32x32x16_f16 v[66:81], v[166:169], v[146:149], v[66:81]
.Lbsk_7182:
	v_add_f32_e32 v84, v108, v84
	v_add_f32_e32 v84, v109, v84
	v_add_f32_e32 v84, v110, v84
	v_add_f32_e32 v84, v111, v84
	v_cvt_pk_f16_f32 v130, v106, v107
	v_cvt_pk_f16_f32 v131, v108, v109
	ds_read_b64_tr_b16 v[98:99], v83 offset:31744
	ds_read_b64_tr_b16 v[100:101], v83 offset:32256
	s_cmp_gt_i32 s43, s56
	s_cbranch_scc1 .Lbsk_7197
	v_mfma_f32_32x32x16_f16 v[50:65], v[162:165], v[146:149], v[50:65]
.Lbsk_7197:
	v_add_f32_e32 v83, v112, v84
	v_add_f32_e32 v83, v113, v83
	v_add_f32_e32 v106, 0, v83
	v_cvt_pk_f16_f32 v132, v110, v111
	v_cvt_pk_f16_f32 v133, v112, v113
	s_add_i32 s49, s48, 2
	s_cmp_ge_u32 s49, s42
	s_cselect_b64 s[20:21], -1, 0
	s_and_b64 vcc, exec, s[20:21]
	s_cbranch_vccnz .LBB2_39
	s_add_i32 s2, s44, s35
	s_mov_b32 s3, m0
	s_mov_b32 m0, s2
	s_nop 0
	global_load_lds_dwordx4 v[218:219], off
	s_mov_b32 m0, s3

.LBB2_61:
	s_waitcnt lgkmcnt(14)
	s_cmp_gt_i32 s43, s52
	s_cbranch_scc1 .Lbsk_7509
	v_mfma_f32_32x32x16_f16 v[2:17], v[142:145], v[202:205], v[2:17]
.Lbsk_7509:
	v_exp_f32_e32 v66, v66
	v_exp_f32_e32 v67, v67
	v_exp_f32_e32 v68, v68
	v_exp_f32_e32 v69, v69
	s_waitcnt lgkmcnt(12)
	s_cmp_gt_i32 s43, s52
	s_cbranch_scc1 .Lbsk_7518
	v_mfma_f32_32x32x16_f16 v[18:33], v[142:145], v[198:201], v[18:33]
.Lbsk_7518:
	v_exp_f32_e32 v70, v70
	v_exp_f32_e32 v71, v71
	v_exp_f32_e32 v72, v72
	v_exp_f32_e32 v73, v73
	v_cndmask_b32_e64 v83, 0, 1, s[22:23]
	v_cmp_ne_u32_e64 s[2:3], 1, v83
	s_andn2_b64 vcc, exec, s[22:23]
	v_add_u32_e32 v83, s40, v224
	s_cbranch_vccnz .LBB2_63
	ds_read_b128 v[190:193], v83
	ds_read_b128 v[186:189], v83 offset:512
.LBB2_63:
	s_waitcnt lgkmcnt(10)
	s_cmp_gt_i32 s43, s52
	s_cbranch_scc1 .Lbsk_7537
	v_mfma_f32_32x32x16_f16 v[2:17], v[138:141], v[194:197], v[2:17]
.Lbsk_7537:
	v_exp_f32_e32 v74, v74
	v_exp_f32_e32 v75, v75
	v_exp_f32_e32 v76, v76
	v_exp_f32_e32 v77, v77
	s_and_b64 vcc, exec, s[2:3]
	s_cbranch_vccnz .LBB2_65
	ds_read_b128 v[182:185], v83 offset:2048
	ds_read_b128 v[178:181], v83 offset:2560
.LBB2_65:
	s_waitcnt lgkmcnt(8)
	s_cmp_gt_i32 s43, s52
	s_cbranch_scc1 .Lbsk_7553
	v_mfma_f32_32x32x16_f16 v[18:33], v[138:141], v[122:125], v[18:33]
.Lbsk_7553:
	v_exp_f32_e32 v78, v78
	v_exp_f32_e32 v79, v79
	v_exp_f32_e32 v80, v80
	v_exp_f32_e32 v81, v81
	s_and_b64 vcc, exec, s[2:3]
	s_cbranch_vccnz .LBB2_67
	ds_read_b128 v[174:177], v83 offset:4096
	ds_read_b128 v[170:173], v83 offset:4608
.LBB2_67:
	s_waitcnt lgkmcnt(6)
	s_cmp_gt_i32 s43, s53
	s_cbranch_scc1 .Lbsk_7569
	v_mfma_f32_32x32x16_f16 v[2:17], v[134:137], v[118:121], v[2:17]
.Lbsk_7569:
	v_exp_f32_e32 v50, v50
	v_exp_f32_e32 v51, v51
	v_exp_f32_e32 v52, v52
	v_exp_f32_e32 v53, v53
	s_and_b64 vcc, exec, s[2:3]
	s_cbranch_vccnz .LBB2_69
	ds_read_b128 v[166:169], v83 offset:6144
	ds_read_b128 v[162:165], v83 offset:6656
.LBB2_69:
	s_waitcnt lgkmcnt(4)
	s_cmp_gt_i32 s43, s53
	s_cbranch_scc1 .Lbsk_7585
	v_mfma_f32_32x32x16_f16 v[18:33], v[134:137], v[114:117], v[18:33]
.Lbsk_7585:
	v_exp_f32_e32 v54, v54
	v_exp_f32_e32 v55, v55
	v_exp_f32_e32 v56, v56
	v_exp_f32_e32 v57, v57
	s_waitcnt lgkmcnt(2)
	s_cmp_gt_i32 s43, s53
	s_cbranch_scc1 .Lbsk_7594
	v_mfma_f32_32x32x16_f16 v[2:17], v[130:133], v[102:105], v[2:17]
.Lbsk_7594:
	v_exp_f32_e32 v58, v58
	v_exp_f32_e32 v59, v59
	v_exp_f32_e32 v60, v60
	v_exp_f32_e32 v61, v61
	s_waitcnt lgkmcnt(0)
	s_cmp_gt_i32 s43, s53
	s_cbranch_scc1 .Lbsk_7603
	v_mfma_f32_32x32x16_f16 v[18:33], v[130:133], v[98:101], v[18:33]
.Lbsk_7603:
	v_exp_f32_e32 v62, v62
	v_exp_f32_e32 v63, v63
	v_exp_f32_e32 v64, v64
	v_exp_f32_e32 v65, v65
	s_mov_b64 s[2:3], -1
	s_and_b64 vcc, exec, s[20:21]
	s_cbranch_vccnz .LBB2_75
	s_andn2_b64 vcc, exec, s[2:3]
	s_cbranch_vccz .LBB2_80

.LBB2_149:
	v_add_u32_e32 v48, s14, v225
	ds_read_b64_tr_b16 v[212:213], v48 offset:24576
	ds_read_b64_tr_b16 v[214:215], v48 offset:25088
	s_waitcnt lgkmcnt(9)
	s_cmp_gt_i32 s27, s52
	s_cbranch_scc1 .Lbsk_10287
	v_mfma_f32_32x32x16_f16 v[128:143], v[204:207], v[156:159], v[32:47]
.Lbsk_10287:
	v_add_f32_e32 v50, v80, v81
	v_add_f32_e32 v50, v82, v50
	v_add_f32_e32 v50, v83, v50
	v_add_f32_e32 v50, v84, v50
	v_add_f32_e32 v50, v85, v50
	v_cvt_pk_f16_f32 v172, v80, v81
	v_cvt_pk_f16_f32 v173, v82, v83
	ds_read_b64_tr_b16 v[204:205], v48 offset:28672
	ds_read_b64_tr_b16 v[206:207], v48 offset:29184
	s_waitcnt lgkmcnt(10)
	s_cmp_gt_i32 s27, s53
	s_cbranch_scc1 .Lbsk_10304
	v_mfma_f32_32x32x16_f16 v[112:127], v[200:203], v[156:159], v[32:47]
.Lbsk_10304:
	v_add_f32_e32 v50, v86, v50
	v_add_f32_e32 v50, v87, v50
	v_add_f32_e32 v50, v88, v50
	v_add_f32_e32 v50, v89, v50
	v_cvt_pk_f16_f32 v174, v84, v85
	v_cvt_pk_f16_f32 v175, v86, v87
	ds_read_b64_tr_b16 v[208:209], v48 offset:25600
	ds_read_b64_tr_b16 v[210:211], v48 offset:26112
	s_waitcnt lgkmcnt(11)
	s_cmp_gt_i32 s27, s52
	s_cbranch_scc1 .Lbsk_10320
	v_mfma_f32_32x32x16_f16 v[128:143], v[196:199], v[152:155], v[128:143]
.Lbsk_10320:
	v_add_f32_e32 v50, v90, v50
	v_add_f32_e32 v50, v91, v50
	v_add_f32_e32 v50, v92, v50
	v_add_f32_e32 v50, v93, v50
	v_cvt_pk_f16_f32 v168, v88, v89
	v_cvt_pk_f16_f32 v169, v90, v91
	ds_read_b64_tr_b16 v[84:85], v48 offset:29696
	ds_read_b64_tr_b16 v[86:87], v48 offset:30208
	s_waitcnt lgkmcnt(12)
	s_cmp_gt_i32 s27, s53
	s_cbranch_scc1 .Lbsk_10336
	v_mfma_f32_32x32x16_f16 v[112:127], v[192:195], v[152:155], v[112:127]
.Lbsk_10336:
	v_add_f32_e32 v50, v94, v50
	v_add_f32_e32 v50, v95, v50
	v_add_f32_e32 v50, v64, v50
	v_add_f32_e32 v50, v65, v50
	v_cvt_pk_f16_f32 v170, v92, v93
	v_cvt_pk_f16_f32 v171, v94, v95
	ds_read_b64_tr_b16 v[80:81], v48 offset:26624
	ds_read_b64_tr_b16 v[82:83], v48 offset:27136
	s_waitcnt lgkmcnt(13)
	s_cmp_gt_i32 s27, s52
	s_cbranch_scc1 .Lbsk_10352
	v_mfma_f32_32x32x16_f16 v[128:143], v[188:191], v[148:151], v[128:143]
.Lbsk_10352:
	v_add_f32_e32 v50, v66, v50
	v_add_f32_e32 v50, v67, v50
	v_add_f32_e32 v50, v68, v50
	v_add_f32_e32 v50, v69, v50
	v_cvt_pk_f16_f32 v164, v64, v65
	v_cvt_pk_f16_f32 v165, v66, v67
	ds_read_b64_tr_b16 v[58:59], v48 offset:30720
	ds_read_b64_tr_b16 v[60:61], v48 offset:31232
	s_waitcnt lgkmcnt(14)
	s_cmp_gt_i32 s27, s53
	s_cbranch_scc1 .Lbsk_10368
	v_mfma_f32_32x32x16_f16 v[112:127], v[184:187], v[148:151], v[112:127]
.Lbsk_10368:
	v_add_f32_e32 v50, v70, v50
	v_add_f32_e32 v50, v71, v50
	v_add_f32_e32 v50, v72, v50
	v_add_f32_e32 v50, v73, v50
	v_cvt_pk_f16_f32 v166, v68, v69
	v_cvt_pk_f16_f32 v167, v70, v71
	ds_read_b64_tr_b16 v[54:55], v48 offset:27648
	ds_read_b64_tr_b16 v[56:57], v48 offset:28160
	s_waitcnt lgkmcnt(14)
	s_cmp_gt_i32 s27, s52
	s_cbranch_scc1 .Lbsk_10384
	v_mfma_f32_32x32x16_f16 v[128:143], v[180:183], v[144:147], v[128:143]
.Lbsk_10384:
	v_add_f32_e32 v50, v74, v50
	v_add_f32_e32 v50, v75, v50
	v_add_f32_e32 v50, v76, v50
	v_add_f32_e32 v64, v77, v50
	v_cvt_pk_f16_f32 v160, v72, v73
	v_cvt_pk_f16_f32 v161, v74, v75
	ds_read_b64_tr_b16 v[50:51], v48 offset:31744
	ds_read_b64_tr_b16 v[52:53], v48 offset:32256
	s_cmp_gt_i32 s27, s53
	s_cbranch_scc1 .Lbsk_10399
	v_mfma_f32_32x32x16_f16 v[112:127], v[176:179], v[144:147], v[112:127]
.Lbsk_10399:
	v_add_f32_e32 v48, v78, v64
	v_add_f32_e32 v48, v79, v48
	v_add_f32_e32 v64, 0, v48
	v_cvt_pk_f16_f32 v162, v76, v77
	v_cvt_pk_f16_f32 v163, v78, v79
	s_add_i32 s2, s20, 1
	s_cmp_ge_u32 s2, s29
	s_cselect_b64 s[14:15], -1, 0
	s_and_b64 vcc, exec, s[14:15]
	s_cbranch_vccnz .LBB2_151
	v_lshl_add_u64 v[66:67], v[222:223], 0, s[8:9]
	s_add_i32 s2, s30, s28
	s_mov_b32 s3, m0
	s_mov_b32 m0, s2
	s_nop 0
	global_load_lds_dwordx4 v[66:67], off
	s_mov_b32 m0, s3

.LBB2_165:
	s_waitcnt lgkmcnt(14)
	s_cmp_gt_i32 s27, s50
	s_cbranch_scc1 .Lbsk_10678
	v_mfma_f32_32x32x16_f16 v[0:15], v[172:175], v[212:215], v[0:15]
.Lbsk_10678:
	v_exp_f32_e32 v128, v128
	v_exp_f32_e32 v129, v129
	v_exp_f32_e32 v130, v130
	v_exp_f32_e32 v131, v131
	s_waitcnt lgkmcnt(12)
	s_cmp_gt_i32 s27, s50
	s_cbranch_scc1 .Lbsk_10687
	v_mfma_f32_32x32x16_f16 v[16:31], v[172:175], v[204:207], v[16:31]
.Lbsk_10687:
	v_exp_f32_e32 v132, v132
	v_exp_f32_e32 v133, v133
	v_exp_f32_e32 v134, v134
	v_exp_f32_e32 v135, v135
	v_add_u32_e32 v64, s31, v224
	ds_read_b128 v[204:207], v64
	ds_read_b128 v[200:203], v64 offset:512
	s_waitcnt lgkmcnt(12)
	s_cmp_gt_i32 s27, s50
	s_cbranch_scc1 .Lbsk_10700
	v_mfma_f32_32x32x16_f16 v[0:15], v[168:171], v[208:211], v[0:15]
.Lbsk_10700:
	v_exp_f32_e32 v136, v136
	v_exp_f32_e32 v137, v137
	v_exp_f32_e32 v138, v138
	v_exp_f32_e32 v139, v139
	ds_read_b128 v[196:199], v64 offset:2048
	ds_read_b128 v[192:195], v64 offset:2560
	s_waitcnt lgkmcnt(12)
	s_cmp_gt_i32 s27, s50
	s_cbranch_scc1 .Lbsk_10712
	v_mfma_f32_32x32x16_f16 v[16:31], v[168:171], v[84:87], v[16:31]
.Lbsk_10712:
	v_exp_f32_e32 v140, v140
	v_exp_f32_e32 v141, v141
	v_exp_f32_e32 v142, v142
	v_exp_f32_e32 v143, v143
	ds_read_b128 v[188:191], v64 offset:4096
	ds_read_b128 v[184:187], v64 offset:4608
	s_waitcnt lgkmcnt(12)
	s_cmp_gt_i32 s27, s51
	s_cbranch_scc1 .Lbsk_10724
	v_mfma_f32_32x32x16_f16 v[0:15], v[164:167], v[80:83], v[0:15]
.Lbsk_10724:
	v_exp_f32_e32 v112, v112
	v_exp_f32_e32 v113, v113
	v_exp_f32_e32 v114, v114
	v_exp_f32_e32 v115, v115
	ds_read_b128 v[180:183], v64 offset:6144
	ds_read_b128 v[176:179], v64 offset:6656
	s_waitcnt lgkmcnt(12)
	s_cmp_gt_i32 s27, s51
	s_cbranch_scc1 .Lbsk_10736
	v_mfma_f32_32x32x16_f16 v[16:31], v[164:167], v[58:61], v[16:31]
.Lbsk_10736:
	v_exp_f32_e32 v116, v116
	v_exp_f32_e32 v117, v117
	v_exp_f32_e32 v118, v118
	v_exp_f32_e32 v119, v119
	s_waitcnt lgkmcnt(10)
	s_cmp_gt_i32 s27, s51
	s_cbranch_scc1 .Lbsk_10745
	v_mfma_f32_32x32x16_f16 v[0:15], v[160:163], v[54:57], v[0:15]
.Lbsk_10745:
	v_exp_f32_e32 v120, v120
	v_exp_f32_e32 v121, v121
	v_exp_f32_e32 v122, v122
	v_exp_f32_e32 v123, v123
	s_waitcnt lgkmcnt(8)
	s_cmp_gt_i32 s27, s51
	s_cbranch_scc1 .Lbsk_10754
	v_mfma_f32_32x32x16_f16 v[16:31], v[160:163], v[50:53], v[16:31]
.Lbsk_10754:
	v_exp_f32_e32 v124, v124
	v_exp_f32_e32 v125, v125
	v_exp_f32_e32 v126, v126
	v_exp_f32_e32 v127, v127
	s_mov_b64 s[16:17], -1
	s_and_b64 vcc, exec, s[14:15]
	s_cbranch_vccnz .LBB2_184
	s_andn2_b64 vcc, exec, s[16:17]
	s_cbranch_vccz .LBB2_189

.LBB2_169:
	v_add_u32_e32 v52, s30, v225
	ds_read_b64_tr_b16 v[216:217], v52 offset:24576
	ds_read_b64_tr_b16 v[218:219], v52 offset:25088
	s_waitcnt lgkmcnt(9)
	s_cmp_gt_i32 s27, s54
	s_cbranch_scc1 .Lbsk_10807
	v_mfma_f32_32x32x16_f16 v[80:95], v[204:207], v[156:159], v[32:47]
.Lbsk_10807:
	v_add_f32_e32 v50, v128, v129
	v_add_f32_e32 v50, v130, v50
	v_add_f32_e32 v50, v131, v50
	v_add_f32_e32 v50, v132, v50
	v_add_f32_e32 v50, v133, v50
	v_cvt_pk_f16_f32 v172, v128, v129
	v_cvt_pk_f16_f32 v173, v130, v131
	ds_read_b64_tr_b16 v[212:213], v52 offset:28672
	ds_read_b64_tr_b16 v[214:215], v52 offset:29184
	s_waitcnt lgkmcnt(10)
	s_cmp_gt_i32 s27, s56
	s_cbranch_scc1 .Lbsk_10824
	v_mfma_f32_32x32x16_f16 v[64:79], v[200:203], v[156:159], v[32:47]
.Lbsk_10824:
	v_add_f32_e32 v50, v134, v50
	v_add_f32_e32 v50, v135, v50
	v_add_f32_e32 v50, v136, v50
	v_add_f32_e32 v50, v137, v50
	v_cvt_pk_f16_f32 v174, v132, v133
	v_cvt_pk_f16_f32 v175, v134, v135
	ds_read_b64_tr_b16 v[208:209], v52 offset:25600
	ds_read_b64_tr_b16 v[210:211], v52 offset:26112
	s_waitcnt lgkmcnt(11)
	s_cmp_gt_i32 s27, s54
	s_cbranch_scc1 .Lbsk_10840
	v_mfma_f32_32x32x16_f16 v[80:95], v[196:199], v[152:155], v[80:95]
.Lbsk_10840:
	v_add_f32_e32 v50, v138, v50
	v_add_f32_e32 v50, v139, v50
	v_add_f32_e32 v50, v140, v50
	v_add_f32_e32 v50, v141, v50
	v_cvt_pk_f16_f32 v168, v136, v137
	v_cvt_pk_f16_f32 v169, v138, v139
	ds_read_b64_tr_b16 v[132:133], v52 offset:29696
	ds_read_b64_tr_b16 v[134:135], v52 offset:30208
	s_waitcnt lgkmcnt(12)
	s_cmp_gt_i32 s27, s56
	s_cbranch_scc1 .Lbsk_10856
	v_mfma_f32_32x32x16_f16 v[64:79], v[192:195], v[152:155], v[64:79]
.Lbsk_10856:
	v_add_f32_e32 v50, v142, v50
	v_add_f32_e32 v50, v143, v50
	v_add_f32_e32 v50, v112, v50
	v_add_f32_e32 v50, v113, v50
	v_cvt_pk_f16_f32 v170, v140, v141
	v_cvt_pk_f16_f32 v171, v142, v143
	ds_read_b64_tr_b16 v[128:129], v52 offset:26624
	ds_read_b64_tr_b16 v[130:131], v52 offset:27136
	s_waitcnt lgkmcnt(13)
	s_cmp_gt_i32 s27, s54
	s_cbranch_scc1 .Lbsk_10872
	v_mfma_f32_32x32x16_f16 v[80:95], v[188:191], v[148:151], v[80:95]
.Lbsk_10872:
	v_add_f32_e32 v50, v114, v50
	v_add_f32_e32 v50, v115, v50
	v_add_f32_e32 v50, v116, v50
	v_add_f32_e32 v50, v117, v50
	v_cvt_pk_f16_f32 v164, v112, v113
	v_cvt_pk_f16_f32 v165, v114, v115
	ds_read_b64_tr_b16 v[58:59], v52 offset:30720
	ds_read_b64_tr_b16 v[60:61], v52 offset:31232
	s_waitcnt lgkmcnt(14)
	s_cmp_gt_i32 s27, s56
	s_cbranch_scc1 .Lbsk_10888
	v_mfma_f32_32x32x16_f16 v[64:79], v[184:187], v[148:151], v[64:79]
.Lbsk_10888:
	v_add_f32_e32 v50, v118, v50
	v_add_f32_e32 v50, v119, v50
	v_add_f32_e32 v50, v120, v50
	v_add_f32_e32 v50, v121, v50
	v_cvt_pk_f16_f32 v166, v116, v117
	v_cvt_pk_f16_f32 v167, v118, v119
	ds_read_b64_tr_b16 v[54:55], v52 offset:27648
	ds_read_b64_tr_b16 v[56:57], v52 offset:28160
	s_waitcnt lgkmcnt(14)
	s_cmp_gt_i32 s27, s54
	s_cbranch_scc1 .Lbsk_10904
	v_mfma_f32_32x32x16_f16 v[80:95], v[180:183], v[144:147], v[80:95]
.Lbsk_10904:
	v_add_f32_e32 v50, v122, v50
	v_add_f32_e32 v50, v123, v50
	v_add_f32_e32 v50, v124, v50
	v_add_f32_e32 v97, v125, v50
	v_cvt_pk_f16_f32 v160, v120, v121
	v_cvt_pk_f16_f32 v161, v122, v123
	ds_read_b64_tr_b16 v[50:51], v52 offset:31744
	ds_read_b64_tr_b16 v[52:53], v52 offset:32256
	s_cmp_gt_i32 s27, s56
	s_cbranch_scc1 .Lbsk_10919
	v_mfma_f32_32x32x16_f16 v[64:79], v[176:179], v[144:147], v[64:79]
.Lbsk_10919:
	v_add_f32_e32 v97, v126, v97
	v_add_f32_e32 v97, v127, v97
	v_add_f32_e32 v112, 0, v97
	v_cvt_pk_f16_f32 v162, v124, v125
	v_cvt_pk_f16_f32 v163, v126, v127
	s_add_i32 s35, s20, 2
	s_cmp_ge_u32 s35, s29
	s_cselect_b64 s[16:17], -1, 0
	s_and_b64 vcc, exec, s[16:17]
	s_cbranch_vccnz .LBB2_171
	s_add_i32 s2, s31, s28
	s_mov_b32 s3, m0
	s_mov_b32 m0, s2
	s_nop 0
	global_load_lds_dwordx4 v[222:223], off
	s_mov_b32 m0, s3

.LBB2_193:
	s_waitcnt lgkmcnt(14)
	s_cmp_gt_i32 s27, s52
	s_cbranch_scc1 .Lbsk_11231
	v_mfma_f32_32x32x16_f16 v[0:15], v[172:175], v[216:219], v[0:15]
.Lbsk_11231:
	v_exp_f32_e32 v80, v80
	v_exp_f32_e32 v81, v81
	v_exp_f32_e32 v82, v82
	v_exp_f32_e32 v83, v83
	s_waitcnt lgkmcnt(12)
	s_cmp_gt_i32 s27, s52
	s_cbranch_scc1 .Lbsk_11240
	v_mfma_f32_32x32x16_f16 v[16:31], v[172:175], v[212:215], v[16:31]
.Lbsk_11240:
	v_exp_f32_e32 v84, v84
	v_exp_f32_e32 v85, v85
	v_exp_f32_e32 v86, v86
	v_exp_f32_e32 v87, v87
	v_cndmask_b32_e64 v48, 0, 1, s[18:19]
	v_cmp_ne_u32_e64 s[2:3], 1, v48
	s_andn2_b64 vcc, exec, s[18:19]
	v_add_u32_e32 v48, s30, v224
	s_cbranch_vccnz .LBB2_195
	ds_read_b128 v[204:207], v48
	ds_read_b128 v[200:203], v48 offset:512
.LBB2_195:
	s_waitcnt lgkmcnt(10)
	s_cmp_gt_i32 s27, s52
	s_cbranch_scc1 .Lbsk_11259
	v_mfma_f32_32x32x16_f16 v[0:15], v[168:171], v[208:211], v[0:15]
.Lbsk_11259:
	v_exp_f32_e32 v88, v88
	v_exp_f32_e32 v89, v89
	v_exp_f32_e32 v90, v90
	v_exp_f32_e32 v91, v91
	s_and_b64 vcc, exec, s[2:3]
	s_cbranch_vccnz .LBB2_197
	ds_read_b128 v[196:199], v48 offset:2048
	ds_read_b128 v[192:195], v48 offset:2560
.LBB2_197:
	s_waitcnt lgkmcnt(8)
	s_cmp_gt_i32 s27, s52
	s_cbranch_scc1 .Lbsk_11275
	v_mfma_f32_32x32x16_f16 v[16:31], v[168:171], v[132:135], v[16:31]
.Lbsk_11275:
	v_exp_f32_e32 v92, v92
	v_exp_f32_e32 v93, v93
	v_exp_f32_e32 v94, v94
	v_exp_f32_e32 v95, v95
	s_and_b64 vcc, exec, s[2:3]
	s_cbranch_vccnz .LBB2_199
	ds_read_b128 v[188:191], v48 offset:4096
	ds_read_b128 v[184:187], v48 offset:4608
.LBB2_199:
	s_waitcnt lgkmcnt(6)
	s_cmp_gt_i32 s27, s53
	s_cbranch_scc1 .Lbsk_11291
	v_mfma_f32_32x32x16_f16 v[0:15], v[164:167], v[128:131], v[0:15]
.Lbsk_11291:
	v_exp_f32_e32 v64, v64
	v_exp_f32_e32 v65, v65
	v_exp_f32_e32 v66, v66
	v_exp_f32_e32 v67, v67
	s_and_b64 vcc, exec, s[2:3]
	s_cbranch_vccnz .LBB2_201
	ds_read_b128 v[180:183], v48 offset:6144
	ds_read_b128 v[176:179], v48 offset:6656
.LBB2_201:
	s_waitcnt lgkmcnt(4)
	s_cmp_gt_i32 s27, s53
	s_cbranch_scc1 .Lbsk_11307
	v_mfma_f32_32x32x16_f16 v[16:31], v[164:167], v[58:61], v[16:31]
.Lbsk_11307:
	v_exp_f32_e32 v68, v68
	v_exp_f32_e32 v69, v69
	v_exp_f32_e32 v70, v70
	v_exp_f32_e32 v71, v71
	s_waitcnt lgkmcnt(2)
	s_cmp_gt_i32 s27, s53
	s_cbranch_scc1 .Lbsk_11316
	v_mfma_f32_32x32x16_f16 v[0:15], v[160:163], v[54:57], v[0:15]
.Lbsk_11316:
	v_exp_f32_e32 v72, v72
	v_exp_f32_e32 v73, v73
	v_exp_f32_e32 v74, v74
	v_exp_f32_e32 v75, v75
	s_waitcnt lgkmcnt(0)
	s_cmp_gt_i32 s27, s53
	s_cbranch_scc1 .Lbsk_11325
	v_mfma_f32_32x32x16_f16 v[16:31], v[160:163], v[50:53], v[16:31]
.Lbsk_11325:
	v_exp_f32_e32 v76, v76
	v_exp_f32_e32 v77, v77
	v_exp_f32_e32 v78, v78
	v_exp_f32_e32 v79, v79
	s_mov_b64 s[2:3], -1
	s_and_b64 vcc, exec, s[16:17]
	s_cbranch_vccnz .LBB2_207
	s_andn2_b64 vcc, exec, s[2:3]
	s_cbranch_vccz .LBB2_212

	.amdhsa_kernel _Z11attn_kernelPKDF16_S0_S0_PDF16_
		.amdhsa_group_segment_fixed_size 0
		.amdhsa_private_segment_fixed_size 0
		.amdhsa_kernarg_size 32
		.amdhsa_user_sgpr_count 2
		.amdhsa_user_sgpr_dispatch_ptr 0
		.amdhsa_user_sgpr_queue_ptr 0
		.amdhsa_user_sgpr_kernarg_segment_ptr 1
		.amdhsa_user_sgpr_dispatch_id 0
		.amdhsa_user_sgpr_kernarg_preload_length 0
		.amdhsa_user_sgpr_kernarg_preload_offset 0
		.amdhsa_user_sgpr_private_segment_size 0
		.amdhsa_uses_dynamic_stack 0
		.amdhsa_enable_private_segment 0
		.amdhsa_system_sgpr_workgroup_id_x 1
		.amdhsa_system_sgpr_workgroup_id_y 0
		.amdhsa_system_sgpr_workgroup_id_z 0
		.amdhsa_system_sgpr_workgroup_info 0
		.amdhsa_system_vgpr_workitem_id 0
		.amdhsa_next_free_vgpr 243
		.amdhsa_next_free_sgpr 57
		.amdhsa_accum_offset 244
		.amdhsa_reserve_vcc 1
		.amdhsa_float_round_mode_32 0
		.amdhsa_float_round_mode_16_64 0
		.amdhsa_float_denorm_mode_32 3
		.amdhsa_float_denorm_mode_16_64 3
		.amdhsa_dx10_clamp 1
		.amdhsa_ieee_mode 1
		.amdhsa_fp16_overflow 0
		.amdhsa_tg_split 0
		.amdhsa_exception_fp_ieee_invalid_op 0
		.amdhsa_exception_fp_denorm_src 0
		.amdhsa_exception_fp_ieee_div_zero 0
		.amdhsa_exception_fp_ieee_overflow 0
		.amdhsa_exception_fp_ieee_underflow 0
		.amdhsa_exception_fp_ieee_inexact 0
		.amdhsa_exception_int_div_zero 0
	.end_amdhsa_kernel

amdhsa.kernels:
  - .agpr_count:     0
    .args:
      - .actual_access:  read_only
        .address_space:  global
        .offset:         0
        .size:           8
        .value_kind:     global_buffer
      - .actual_access:  read_only
        .address_space:  global
        .offset:         8
        .size:           8
        .value_kind:     global_buffer
      - .actual_access:  read_only
        .address_space:  global
        .offset:         16
        .size:           8
        .value_kind:     global_buffer
      - .actual_access:  read_only
        .address_space:  global
        .offset:         24
        .size:           8
        .value_kind:     global_buffer
      - .actual_access:  read_only
        .address_space:  global
        .offset:         32
        .size:           8
        .value_kind:     global_buffer
      - .actual_access:  read_only
        .address_space:  global
        .offset:         40
        .size:           8
        .value_kind:     global_buffer
      - .address_space:  global
        .offset:         48
        .size:           8
        .value_kind:     global_buffer
      - .address_space:  global
        .offset:         56
        .size:           8
        .value_kind:     global_buffer
      - .address_space:  global
        .offset:         64
        .size:           8
        .value_kind:     global_buffer
      - .address_space:  global
        .offset:         72
        .size:           8
        .value_kind:     global_buffer
    .group_segment_fixed_size: 0
    .kernarg_segment_align: 8
    .kernarg_segment_size: 80
    .language:       OpenCL C
    .language_version:
      - 2
      - 0
    .max_flat_workgroup_size: 256
    .name:           _Z11prep_kernelPKfPKiS0_S0_S0_S0_PtS3_S3_P15HIP_vector_typeIfLj2EE
    .private_segment_fixed_size: 0
    .sgpr_count:     40
    .sgpr_spill_count: 0
    .symbol:         _Z11prep_kernelPKfPKiS0_S0_S0_S0_PtS3_S3_P15HIP_vector_typeIfLj2EE.kd
    .uniform_work_group_size: 1
    .uses_dynamic_stack: false
    .vgpr_count:     40
    .vgpr_spill_count: 0
    .wavefront_size: 64
  - .agpr_count:     0
    .args:
      - .offset:         0
        .size:           32
        .value_kind:     by_value
      - .offset:         32
        .size:           24
        .value_kind:     by_value
      - .offset:         56
        .size:           32
        .value_kind:     by_value
      - .offset:         88
        .size:           24
        .value_kind:     by_value
      - .offset:         112
        .size:           4
        .value_kind:     hidden_block_count_x
      - .offset:         116
        .size:           4
        .value_kind:     hidden_block_count_y
      - .offset:         120
        .size:           4
        .value_kind:     hidden_block_count_z
      - .offset:         124
        .size:           2
        .value_kind:     hidden_group_size_x
      - .offset:         126
        .size:           2
        .value_kind:     hidden_group_size_y
      - .offset:         128
        .size:           2
        .value_kind:     hidden_group_size_z
      - .offset:         130
        .size:           2
        .value_kind:     hidden_remainder_x
      - .offset:         132
        .size:           2
        .value_kind:     hidden_remainder_y
      - .offset:         134
        .size:           2
        .value_kind:     hidden_remainder_z
      - .offset:         152
        .size:           8
        .value_kind:     hidden_global_offset_x
      - .offset:         160
        .size:           8
        .value_kind:     hidden_global_offset_y
      - .offset:         168
        .size:           8
        .value_kind:     hidden_global_offset_z
      - .offset:         176
        .size:           2
        .value_kind:     hidden_grid_dims
      - .offset:         232
        .size:           4
        .value_kind:     hidden_dynamic_lds_size
    .group_segment_fixed_size: 0
    .kernarg_segment_align: 8
    .kernarg_segment_size: 368
    .language:       OpenCL C
    .language_version:
      - 2
      - 0
    .max_flat_workgroup_size: 512
    .name:           _Z10qkv_kernelN3pg84GemmENS_7EpiRopeEN2hg4GemmENS2_7EpiRopeE
    .private_segment_fixed_size: 0
    .sgpr_count:     99
    .sgpr_spill_count: 0
    .symbol:         _Z10qkv_kernelN3pg84GemmENS_7EpiRopeEN2hg4GemmENS2_7EpiRopeE.kd
    .uniform_work_group_size: 1
    .uses_dynamic_stack: false
    .vgpr_count:     240
    .vgpr_spill_count: 0
    .wavefront_size: 64
  - .agpr_count:     0
    .args:
      - .address_space:  global
        .offset:         0
        .size:           8
        .value_kind:     global_buffer
      - .address_space:  global
        .offset:         8
        .size:           8
        .value_kind:     global_buffer
      - .address_space:  global
        .offset:         16
        .size:           8
        .value_kind:     global_buffer
      - .address_space:  global
        .offset:         24
        .size:           8
        .value_kind:     global_buffer
    .group_segment_fixed_size: 0
    .kernarg_segment_align: 8
    .kernarg_segment_size: 32
    .language:       OpenCL C
    .language_version:
      - 2
      - 0
    .max_flat_workgroup_size: 512
    .name:           _Z11attn_kernelPKDF16_S0_S0_PDF16_
    .private_segment_fixed_size: 0
    .sgpr_count:     63
    .sgpr_spill_count: 0
    .symbol:         _Z11attn_kernelPKDF16_S0_S0_PDF16_.kd
    .uniform_work_group_size: 1
    .uses_dynamic_stack: false
    .vgpr_count:     243
    .vgpr_spill_count: 0
    .wavefront_size: 64
  - .agpr_count:     0
    .args:
      - .offset:         0
        .size:           32
        .value_kind:     by_value
      - .offset:         32
        .size:           16
        .value_kind:     by_value
      - .offset:         48
        .size:           4
        .value_kind:     hidden_block_count_x
      - .offset:         52
        .size:           4
        .value_kind:     hidden_block_count_y
      - .offset:         56
        .size:           4
        .value_kind:     hidden_block_count_z
      - .offset:         60
        .size:           2
        .value_kind:     hidden_group_size_x
      - .offset:         62
        .size:           2
        .value_kind:     hidden_group_size_y
      - .offset:         64
        .size:           2
        .value_kind:     hidden_group_size_z
      - .offset:         66
        .size:           2
        .value_kind:     hidden_remainder_x
      - .offset:         68
        .size:           2
        .value_kind:     hidden_remainder_y
      - .offset:         70
        .size:           2
        .value_kind:     hidden_remainder_z
      - .offset:         88
        .size:           8
        .value_kind:     hidden_global_offset_x
      - .offset:         96
        .size:           8
        .value_kind:     hidden_global_offset_y
      - .offset:         104
        .size:           8
        .value_kind:     hidden_global_offset_z
      - .offset:         112
        .size:           2
        .value_kind:     hidden_grid_dims
      - .offset:         168
        .size:           4
        .value_kind:     hidden_dynamic_lds_size
    .group_segment_fixed_size: 0
    .kernarg_segment_align: 8
    .kernarg_segment_size: 304
    .language:       OpenCL C
    .language_version:
      - 2
      - 0
    .max_flat_workgroup_size: 512
    .name:           _Z12hgemm_kernelIN2hg6EpiF32EEvNS0_4GemmET_
    .private_segment_fixed_size: 0
    .sgpr_count:     62
    .sgpr_spill_count: 0
    .symbol:         _Z12hgemm_kernelIN2hg6EpiF32EEvNS0_4GemmET_.kd
    .uniform_work_group_size: 1
    .uses_dynamic_stack: false
    .vgpr_count:     138
    .vgpr_spill_count: 0
    .wavefront_size: 64
